# rope epilogue: stores back to permlane16-paired dwordx4 without the ds_bpermute transposition (table loads stay transposed)
# baseline (speedup 1.0000x reference)
; #define PG8_ST8(rs, b0, p, v) __builtin_amdgcn_raw_buffer_store_b64(v, rs, (int)((const char*)(p) - (const char*)(b0)), 0, 16)
; __device__ __forceinline__ unsigned cvt_pk_bf16(float lo, float hi) { unsigned r; asm volatile("v_cvt_pk_bf16_f32 %0, %1, %2" : "=v"(r) : "v"(lo), "v"(hi)); return r; }
;     __device__ __forceinline__ void operator()(const f32x4 (&acc)[2][2][4][2], const Unit& u, int wr, int wc, int fr, int fq) const {
;     ...
;             const float sc = (pn <= 6 || (pn >= 9 && pn <= 11)) ? qscale : 1.0f;
;             const int f = 16 * (wc & 1) + 4 * fq, col0 = pn * BM + 64 * (wc >> 1) + f;
; #pragma unroll
;             for (int ai = 0; ai < 2; ++ai) {
;                 f32x4 c4[4], s4[4];
; #pragma unroll
;                 for (int m = 0; m < 4; ++m) { const int row = row0 + ai * HALF + m * 16; c4[m] = *(const f32x4*)(rc + (size_t)row * 32 + f); s4[m] = *(const f32x4*)(rs + (size_t)row * 32 + f); }
;                 asm volatile("" ::: "memory");
; #pragma unroll
;                 for (int m = 0; m < 4; ++m) { const int row = row0 + ai * HALF + m * 16;
;                     const f32x4 cc = c4[m] * sc, ss = s4[m] * sc;
;                     bf16_t* rowp = P + (size_t)row * ldp + col0;
; #pragma unroll
;                     for (int bj = 0; bj < 2; ++bj) { const f32x4 x1 = acc[ai][bj][m][0], x2 = acc[ai][bj][m][1]; const f32x4 o1 = x1 * cc - x2 * ss, o2 = x2 * cc + x1 * ss;
;                         u32x2 w1, w2; w1.x = cvt_pk_bf16(o1[0], o1[1]); w1.y = cvt_pk_bf16(o1[2], o1[3]); w2.x = cvt_pk_bf16(o2[0], o2[1]); w2.y = cvt_pk_bf16(o2[2], o2[3]);
;                         PG8_ST8(rsp_, P, rowp + bj * HALF, w1); PG8_ST8(rsp_, P, rowp + bj * HALF + 32, w2); } }
.LBB0_230:
	v_lshl_add_u32 v164, s27, 8, v175
	s_add_i32 s27, s62, s56
	s_cmp_gt_i32 s27, 3
	s_mov_b64 s[34:35], -1
	s_cbranch_scc0 .LBB0_237
	s_cmp_lg_u32 s27, 8
	s_cselect_b64 s[34:35], -1, 0
	s_cmp_lt_u32 s27, 15
	s_cselect_b64 s[36:37], -1, 0
	s_and_b64 s[36:37], s[34:35], s[36:37]
	s_mov_b64 s[34:35], -1
	s_and_b64 vcc, exec, s[36:37]
	v_add_u32_e32 v172, 0x80, v164
	v_add_u32_e32 v170, 0x90, v164
	v_add_u32_e32 v168, 0xa0, v164
	v_add_u32_e32 v166, 0xb0, v164
	s_cbranch_vccz .LBB0_233
	v_lshrrev_b32_e32 v252, 2, v215
	v_and_b32_e32 v245, 15, v215
	v_sub_u32_e32 v252, v252, v245
	v_lshlrev_b32_e32 v245, 4, v245
	v_lshrrev_b32_e32 v246, 4, v215
	v_lshl_or_b32 v245, v246, 2, v245
	v_and_b32_e32 v248, 3, v215
	v_sub_u32_e32 v246, v248, v246
	v_lshlrev_b32_e32 v252, 7, v252
	v_lshl_add_u32 v248, v246, 4, v252
	v_ashrrev_i32_e32 v249, 31, v248
	v_lshl_add_u64 v[246:247], v[154:155], 0, v[248:249]
	v_lshl_add_u64 v[248:249], v[156:157], 0, v[248:249]
	s_cmp_lt_u32 s27, 7
	s_cselect_b64 s[34:35], -1, 0
	s_add_i32 s36, s27, -9
	s_cmp_lt_u32 s36, 3
	s_cselect_b64 s[36:37], -1, 0
	s_or_b64 vcc, s[34:35], s[36:37]
	v_mov_b32_e32 v132, 0x3e38aa3b
	v_ashrrev_i32_e32 v165, 31, v164
	v_cndmask_b32_e32 v174, 1.0, v132, vcc
	v_lshlrev_b64 v[132:133], 7, v[164:165]
	v_lshl_add_u64 v[134:135], v[246:247], 0, v[132:133]
	v_lshl_add_u64 v[132:133], v[248:249], 0, v[132:133]
	global_load_dwordx4 v[176:179], v[134:135], off
	global_load_dwordx4 v[184:187], v[132:133], off
	v_or_b32_e32 v192, 16, v164
	v_ashrrev_i32_e32 v193, 31, v192
	v_lshlrev_b64 v[132:133], 7, v[192:193]
	v_lshl_add_u64 v[134:135], v[246:247], 0, v[132:133]
	v_lshl_add_u64 v[132:133], v[248:249], 0, v[132:133]
	global_load_dwordx4 v[188:191], v[134:135], off
	global_load_dwordx4 v[218:221], v[132:133], off
	v_or_b32_e32 v182, 32, v164
	v_ashrrev_i32_e32 v183, 31, v182
	v_lshlrev_b64 v[132:133], 7, v[182:183]
	v_lshl_add_u64 v[134:135], v[246:247], 0, v[132:133]
	v_lshl_add_u64 v[132:133], v[248:249], 0, v[132:133]
	global_load_dwordx4 v[144:147], v[134:135], off
	global_load_dwordx4 v[140:143], v[132:133], off
	v_or_b32_e32 v180, 48, v164
	v_ashrrev_i32_e32 v181, 31, v180
	v_lshlrev_b64 v[132:133], 7, v[180:181]
	v_lshl_add_u64 v[134:135], v[246:247], 0, v[132:133]
	v_lshl_add_u64 v[132:133], v[248:249], 0, v[132:133]
	global_load_dwordx4 v[136:139], v[134:135], off
	s_movk_i32 s36, 0x2400
	global_load_dwordx4 v[132:135], v[132:133], off
	v_ashrrev_i32_e32 v173, 31, v172
	v_ashrrev_i32_e32 v171, 31, v170
	v_ashrrev_i32_e32 v169, 31, v168
	v_ashrrev_i32_e32 v167, 31, v166
	s_waitcnt vmcnt(0)
	ds_bpermute_b32 v176, v245, v176
	ds_bpermute_b32 v177, v245, v177
	ds_bpermute_b32 v178, v245, v178
	ds_bpermute_b32 v179, v245, v179
	ds_bpermute_b32 v184, v245, v184
	ds_bpermute_b32 v185, v245, v185
	ds_bpermute_b32 v186, v245, v186
	ds_bpermute_b32 v187, v245, v187
	ds_bpermute_b32 v188, v245, v188
	ds_bpermute_b32 v189, v245, v189
	ds_bpermute_b32 v190, v245, v190
	ds_bpermute_b32 v191, v245, v191
	ds_bpermute_b32 v218, v245, v218
	ds_bpermute_b32 v219, v245, v219
	ds_bpermute_b32 v220, v245, v220
	ds_bpermute_b32 v221, v245, v221
	ds_bpermute_b32 v144, v245, v144
	ds_bpermute_b32 v145, v245, v145
	ds_bpermute_b32 v146, v245, v146
	ds_bpermute_b32 v147, v245, v147
	ds_bpermute_b32 v140, v245, v140
	ds_bpermute_b32 v141, v245, v141
	ds_bpermute_b32 v142, v245, v142
	ds_bpermute_b32 v143, v245, v143
	ds_bpermute_b32 v136, v245, v136
	ds_bpermute_b32 v137, v245, v137
	ds_bpermute_b32 v138, v245, v138
	ds_bpermute_b32 v139, v245, v139
	ds_bpermute_b32 v132, v245, v132
	ds_bpermute_b32 v133, v245, v133
	ds_bpermute_b32 v134, v245, v134
	ds_bpermute_b32 v135, v245, v135
	s_waitcnt lgkmcnt(0)
	v_pk_mul_f32 v[198:199], v[174:175], v[178:179] op_sel_hi:[0,1]
	v_pk_mul_f32 v[186:187], v[174:175], v[186:187] op_sel_hi:[0,1]
	v_pk_mul_f32 v[184:185], v[174:175], v[184:185] op_sel_hi:[0,1]
	v_pk_mul_f32 v[200:201], v[174:175], v[176:177] op_sel_hi:[0,1]
	v_mov_b64_e32 v[176:177], s[20:21]
	v_pk_mul_f32 v[208:209], v[118:119], v[186:187]
	v_pk_mul_f32 v[222:223], v[116:117], v[184:185]
	v_mad_i64_i32 v[204:205], s[34:35], v164, s36, v[176:177]
	v_lshl_or_b32 v178, s27, 9, v202
	v_mov_b32_e32 v179, v2
	v_bfe_u32 v244, v215, 4, 1
	v_mul_u32_u24_e32 v244, 56, v244
	v_add_u32_e32 v178, v178, v244
	v_pk_fma_f32 v[208:209], v[126:127], v[198:199], v[208:209] neg_lo:[0,0,1] neg_hi:[0,0,1]
	v_pk_fma_f32 v[222:223], v[124:125], v[200:201], v[222:223] neg_lo:[0,0,1] neg_hi:[0,0,1]
	v_pk_mul_f32 v[224:225], v[126:127], v[186:187]
	v_pk_mul_f32 v[226:227], v[124:125], v[184:185]
	v_lshl_add_u64 v[204:205], v[204:205], 0, v[178:179]
	v_pk_fma_f32 v[224:225], v[118:119], v[198:199], v[224:225]
	v_pk_fma_f32 v[226:227], v[116:117], v[200:201], v[226:227]
	v_cvt_pk_bf16_f32 v228, v222, v223
	v_cvt_pk_bf16_f32 v229, v208, v209
	v_mad_i64_i32 v[192:193], s[34:35], v192, s36, v[176:177]
	v_cvt_pk_bf16_f32 v230, v226, v227
	v_cvt_pk_bf16_f32 v231, v224, v225
	s_nop 1
	v_permlane16_swap_b32_e32 v228, v230
	v_permlane16_swap_b32_e32 v229, v231
	global_store_dwordx4 v[204:205], v[228:231], off
	v_pk_mul_f32 v[208:209], v[122:123], v[186:187]
	v_pk_mul_f32 v[222:223], v[120:121], v[184:185]
	v_pk_mul_f32 v[186:187], v[130:131], v[186:187]
	v_pk_mul_f32 v[184:185], v[128:129], v[184:185]
	v_pk_fma_f32 v[186:187], v[122:123], v[198:199], v[186:187]
	v_pk_fma_f32 v[184:185], v[120:121], v[200:201], v[184:185]
	v_pk_fma_f32 v[208:209], v[130:131], v[198:199], v[208:209] neg_lo:[0,0,1] neg_hi:[0,0,1]
	v_pk_fma_f32 v[222:223], v[128:129], v[200:201], v[222:223] neg_lo:[0,0,1] neg_hi:[0,0,1]
	v_lshl_add_u64 v[192:193], v[192:193], 0, v[178:179]
; #define PG8_ST8(rs, b0, p, v) __builtin_amdgcn_raw_buffer_store_b64(v, rs, (int)((const char*)(p) - (const char*)(b0)), 0, 16)
; __device__ __forceinline__ unsigned cvt_pk_bf16(float lo, float hi) { unsigned r; asm volatile("v_cvt_pk_bf16_f32 %0, %1, %2" : "=v"(r) : "v"(lo), "v"(hi)); return r; }
;     __device__ __forceinline__ void operator()(const f32x4 (&acc)[2][2][4][2], const Unit& u, int wr, int wc, int fr, int fq) const {
;     ...
;                 for (int m = 0; m < 4; ++m) { const int row = row0 + ai * HALF + m * 16;
;                     const f32x4 cc = c4[m] * sc, ss = s4[m] * sc;
;                     bf16_t* rowp = P + (size_t)row * ldp + col0;
; #pragma unroll
;                     for (int bj = 0; bj < 2; ++bj) { const f32x4 x1 = acc[ai][bj][m][0], x2 = acc[ai][bj][m][1]; const f32x4 o1 = x1 * cc - x2 * ss, o2 = x2 * cc + x1 * ss;
;                         u32x2 w1, w2; w1.x = cvt_pk_bf16(o1[0], o1[1]); w1.y = cvt_pk_bf16(o1[2], o1[3]); w2.x = cvt_pk_bf16(o2[0], o2[1]); w2.y = cvt_pk_bf16(o2[2], o2[3]);
;                         PG8_ST8(rsp_, P, rowp + bj * HALF, w1); PG8_ST8(rsp_, P, rowp + bj * HALF + 32, w2); } }
	v_cvt_pk_bf16_f32 v232, v222, v223
	v_cvt_pk_bf16_f32 v233, v208, v209
	v_cvt_pk_bf16_f32 v234, v184, v185
	v_cvt_pk_bf16_f32 v235, v186, v187
	v_pk_mul_f32 v[186:187], v[174:175], v[190:191] op_sel_hi:[0,1]
	v_pk_mul_f32 v[190:191], v[174:175], v[218:219] op_sel_hi:[0,1]
	s_nop 1
	v_permlane16_swap_b32_e32 v232, v234
	v_permlane16_swap_b32_e32 v233, v235
	global_store_dwordx4 v[204:205], v[232:235], off offset:256
	v_pk_mul_f32 v[184:185], v[174:175], v[188:189] op_sel_hi:[0,1]
	v_pk_mul_f32 v[188:189], v[174:175], v[220:221] op_sel_hi:[0,1]
	v_pk_mul_f32 v[198:199], v[100:101], v[190:191]
	v_pk_mul_f32 v[200:201], v[102:103], v[188:189]
	v_pk_fma_f32 v[198:199], v[108:109], v[184:185], v[198:199] neg_lo:[0,0,1] neg_hi:[0,0,1]
	v_pk_fma_f32 v[200:201], v[110:111], v[186:187], v[200:201] neg_lo:[0,0,1] neg_hi:[0,0,1]
	v_pk_mul_f32 v[204:205], v[108:109], v[190:191]
	v_pk_mul_f32 v[208:209], v[110:111], v[188:189]
	v_cvt_pk_bf16_f32 v236, v198, v199
	v_cvt_pk_bf16_f32 v237, v200, v201
	v_pk_fma_f32 v[204:205], v[100:101], v[184:185], v[204:205]
	v_pk_fma_f32 v[208:209], v[102:103], v[186:187], v[208:209]
	v_cvt_pk_bf16_f32 v238, v204, v205
	v_pk_mul_f32 v[142:143], v[174:175], v[142:143] op_sel_hi:[0,1]
	v_cvt_pk_bf16_f32 v239, v208, v209
	s_nop 1
	v_permlane16_swap_b32_e32 v236, v238
	v_permlane16_swap_b32_e32 v237, v239
	global_store_dwordx4 v[192:193], v[236:239], off
	v_pk_mul_f32 v[198:199], v[104:105], v[190:191]
	v_pk_mul_f32 v[190:191], v[112:113], v[190:191]
	v_pk_mul_f32 v[200:201], v[106:107], v[188:189]
	v_pk_fma_f32 v[198:199], v[112:113], v[184:185], v[198:199] neg_lo:[0,0,1] neg_hi:[0,0,1]
	v_pk_mul_f32 v[188:189], v[114:115], v[188:189]
	v_pk_fma_f32 v[184:185], v[104:105], v[184:185], v[190:191]
	v_pk_fma_f32 v[200:201], v[114:115], v[186:187], v[200:201] neg_lo:[0,0,1] neg_hi:[0,0,1]
	v_pk_fma_f32 v[186:187], v[106:107], v[186:187], v[188:189]
	v_cvt_pk_bf16_f32 v240, v198, v199
	v_cvt_pk_bf16_f32 v241, v200, v201
	v_cvt_pk_bf16_f32 v242, v184, v185
	v_pk_mul_f32 v[140:141], v[174:175], v[140:141] op_sel_hi:[0,1]
	v_cvt_pk_bf16_f32 v243, v186, v187
	s_nop 1
	v_permlane16_swap_b32_e32 v240, v242
	v_permlane16_swap_b32_e32 v241, v243
	global_store_dwordx4 v[192:193], v[240:243], off offset:256
	v_pk_mul_f32 v[144:145], v[174:175], v[144:145] op_sel_hi:[0,1]
	v_pk_mul_f32 v[146:147], v[174:175], v[146:147] op_sel_hi:[0,1]
	v_pk_mul_f32 v[184:185], v[84:85], v[140:141]
	v_pk_mul_f32 v[186:187], v[86:87], v[142:143]
	v_mad_i64_i32 v[182:183], s[34:35], v182, s36, v[176:177]
	v_pk_fma_f32 v[186:187], v[94:95], v[146:147], v[186:187] neg_lo:[0,0,1] neg_hi:[0,0,1]
	v_pk_fma_f32 v[184:185], v[92:93], v[144:145], v[184:185] neg_lo:[0,0,1] neg_hi:[0,0,1]
	v_pk_mul_f32 v[188:189], v[92:93], v[140:141]
	v_pk_mul_f32 v[190:191], v[94:95], v[142:143]
	v_lshl_add_u64 v[182:183], v[182:183], 0, v[178:179]
	v_pk_fma_f32 v[190:191], v[86:87], v[146:147], v[190:191]
	v_pk_fma_f32 v[188:189], v[84:85], v[144:145], v[188:189]
	v_cvt_pk_bf16_f32 v228, v184, v185
	v_cvt_pk_bf16_f32 v229, v186, v187
	v_pk_mul_f32 v[134:135], v[174:175], v[134:135] op_sel_hi:[0,1]
	v_cvt_pk_bf16_f32 v230, v188, v189
	v_cvt_pk_bf16_f32 v231, v190, v191
	s_nop 1
	v_permlane16_swap_b32_e32 v228, v230
	v_permlane16_swap_b32_e32 v229, v231
	global_store_dwordx4 v[182:183], v[228:231], off
	v_pk_mul_f32 v[184:185], v[88:89], v[140:141]
	v_pk_mul_f32 v[186:187], v[90:91], v[142:143]
	v_pk_mul_f32 v[140:141], v[96:97], v[140:141]
	v_pk_mul_f32 v[142:143], v[98:99], v[142:143]
	v_pk_fma_f32 v[186:187], v[98:99], v[146:147], v[186:187] neg_lo:[0,0,1] neg_hi:[0,0,1]
	v_pk_fma_f32 v[184:185], v[96:97], v[144:145], v[184:185] neg_lo:[0,0,1] neg_hi:[0,0,1]
	v_pk_fma_f32 v[142:143], v[90:91], v[146:147], v[142:143]
	v_pk_fma_f32 v[140:141], v[88:89], v[144:145], v[140:141]
	v_cvt_pk_bf16_f32 v232, v184, v185
	v_cvt_pk_bf16_f32 v233, v186, v187
	v_pk_mul_f32 v[132:133], v[174:175], v[132:133] op_sel_hi:[0,1]
	v_cvt_pk_bf16_f32 v234, v140, v141
	v_cvt_pk_bf16_f32 v235, v142, v143
	s_nop 1
	v_permlane16_swap_b32_e32 v232, v234
	v_permlane16_swap_b32_e32 v233, v235
	global_store_dwordx4 v[182:183], v[232:235], off offset:256
	v_pk_mul_f32 v[136:137], v[174:175], v[136:137] op_sel_hi:[0,1]
	v_pk_mul_f32 v[138:139], v[174:175], v[138:139] op_sel_hi:[0,1]
	v_pk_mul_f32 v[142:143], v[68:69], v[132:133]
	v_pk_mul_f32 v[144:145], v[70:71], v[134:135]
	v_mad_i64_i32 v[140:141], s[34:35], v180, s36, v[176:177]
	v_pk_fma_f32 v[144:145], v[78:79], v[138:139], v[144:145] neg_lo:[0,0,1] neg_hi:[0,0,1]
	v_pk_fma_f32 v[142:143], v[76:77], v[136:137], v[142:143] neg_lo:[0,0,1] neg_hi:[0,0,1]
	v_pk_mul_f32 v[146:147], v[76:77], v[132:133]
	v_pk_mul_f32 v[180:181], v[78:79], v[134:135]
	v_lshl_add_u64 v[140:141], v[140:141], 0, v[178:179]
	v_pk_fma_f32 v[180:181], v[70:71], v[138:139], v[180:181]
	v_pk_fma_f32 v[146:147], v[68:69], v[136:137], v[146:147]
	v_cvt_pk_bf16_f32 v236, v142, v143
	v_cvt_pk_bf16_f32 v237, v144, v145
	v_lshlrev_b64 v[184:185], 7, v[168:169]
	v_cvt_pk_bf16_f32 v238, v146, v147
	v_cvt_pk_bf16_f32 v239, v180, v181
	s_nop 1
	v_permlane16_swap_b32_e32 v236, v238
	v_permlane16_swap_b32_e32 v237, v239
	global_store_dwordx4 v[140:141], v[236:239], off
	v_pk_mul_f32 v[142:143], v[72:73], v[132:133]
	v_pk_mul_f32 v[144:145], v[74:75], v[134:135]
	v_pk_mul_f32 v[132:133], v[80:81], v[132:133]
	v_pk_fma_f32 v[144:145], v[82:83], v[138:139], v[144:145] neg_lo:[0,0,1] neg_hi:[0,0,1]
	v_pk_fma_f32 v[142:143], v[80:81], v[136:137], v[142:143] neg_lo:[0,0,1] neg_hi:[0,0,1]
	v_pk_mul_f32 v[134:135], v[82:83], v[134:135]
	v_pk_fma_f32 v[132:133], v[72:73], v[136:137], v[132:133]
	v_cvt_pk_bf16_f32 v240, v142, v143
	v_cvt_pk_bf16_f32 v241, v144, v145
	v_pk_fma_f32 v[134:135], v[74:75], v[138:139], v[134:135]
	v_cvt_pk_bf16_f32 v242, v132, v133
	v_lshlrev_b64 v[144:145], 7, v[170:171]
	v_cvt_pk_bf16_f32 v243, v134, v135
	s_nop 1
	v_permlane16_swap_b32_e32 v240, v242
	v_permlane16_swap_b32_e32 v241, v243
	global_store_dwordx4 v[140:141], v[240:243], off offset:256
	v_lshlrev_b64 v[136:137], 7, v[172:173]
	v_lshl_add_u64 v[132:133], v[246:247], 0, v[136:137]
	v_lshl_add_u64 v[136:137], v[248:249], 0, v[136:137]
	global_load_dwordx4 v[132:135], v[132:133], off
	v_lshl_add_u64 v[140:141], v[246:247], 0, v[144:145]
	global_load_dwordx4 v[136:139], v[136:137], off
	v_lshl_add_u64 v[144:145], v[248:249], 0, v[144:145]
	global_load_dwordx4 v[140:143], v[140:141], off
	v_lshl_add_u64 v[180:181], v[246:247], 0, v[184:185]
	global_load_dwordx4 v[144:147], v[144:145], off
	v_lshl_add_u64 v[184:185], v[248:249], 0, v[184:185]
	global_load_dwordx4 v[180:183], v[180:181], off
	v_lshlrev_b64 v[192:193], 7, v[166:167]
	global_load_dwordx4 v[184:187], v[184:185], off
	v_lshl_add_u64 v[188:189], v[246:247], 0, v[192:193]
	v_lshl_add_u64 v[192:193], v[248:249], 0, v[192:193]
	global_load_dwordx4 v[188:191], v[188:189], off
	global_load_dwordx4 v[218:221], v[192:193], off
	s_waitcnt vmcnt(0)
; #define PG8_ST8(rs, b0, p, v) __builtin_amdgcn_raw_buffer_store_b64(v, rs, (int)((const char*)(p) - (const char*)(b0)), 0, 16)
; __device__ __forceinline__ unsigned cvt_pk_bf16(float lo, float hi) { unsigned r; asm volatile("v_cvt_pk_bf16_f32 %0, %1, %2" : "=v"(r) : "v"(lo), "v"(hi)); return r; }
;     __device__ __forceinline__ void operator()(const f32x4 (&acc)[2][2][4][2], const Unit& u, int wr, int wc, int fr, int fq) const {
;     ...
;             for (int ai = 0; ai < 2; ++ai) {
;                 f32x4 c4[4], s4[4];
; #pragma unroll
;                 for (int m = 0; m < 4; ++m) { const int row = row0 + ai * HALF + m * 16; c4[m] = *(const f32x4*)(rc + (size_t)row * 32 + f); s4[m] = *(const f32x4*)(rs + (size_t)row * 32 + f); }
;                 asm volatile("" ::: "memory");
; #pragma unroll
;                 for (int m = 0; m < 4; ++m) { const int row = row0 + ai * HALF + m * 16;
;                     const f32x4 cc = c4[m] * sc, ss = s4[m] * sc;
;                     bf16_t* rowp = P + (size_t)row * ldp + col0;
; #pragma unroll
;                     for (int bj = 0; bj < 2; ++bj) { const f32x4 x1 = acc[ai][bj][m][0], x2 = acc[ai][bj][m][1]; const f32x4 o1 = x1 * cc - x2 * ss, o2 = x2 * cc + x1 * ss;
;                         u32x2 w1, w2; w1.x = cvt_pk_bf16(o1[0], o1[1]); w1.y = cvt_pk_bf16(o1[2], o1[3]); w2.x = cvt_pk_bf16(o2[0], o2[1]); w2.y = cvt_pk_bf16(o2[2], o2[3]);
;                         PG8_ST8(rsp_, P, rowp + bj * HALF, w1); PG8_ST8(rsp_, P, rowp + bj * HALF + 32, w2); } }
	ds_bpermute_b32 v132, v245, v132
	ds_bpermute_b32 v133, v245, v133
	ds_bpermute_b32 v134, v245, v134
	ds_bpermute_b32 v135, v245, v135
	ds_bpermute_b32 v136, v245, v136
	ds_bpermute_b32 v137, v245, v137
	ds_bpermute_b32 v138, v245, v138
	ds_bpermute_b32 v139, v245, v139
	ds_bpermute_b32 v140, v245, v140
	ds_bpermute_b32 v141, v245, v141
	ds_bpermute_b32 v142, v245, v142
	ds_bpermute_b32 v143, v245, v143
	ds_bpermute_b32 v144, v245, v144
	ds_bpermute_b32 v145, v245, v145
	ds_bpermute_b32 v146, v245, v146
	ds_bpermute_b32 v147, v245, v147
	ds_bpermute_b32 v180, v245, v180
	ds_bpermute_b32 v181, v245, v181
	ds_bpermute_b32 v182, v245, v182
	ds_bpermute_b32 v183, v245, v183
	ds_bpermute_b32 v184, v245, v184
	ds_bpermute_b32 v185, v245, v185
	ds_bpermute_b32 v186, v245, v186
	ds_bpermute_b32 v187, v245, v187
	ds_bpermute_b32 v188, v245, v188
	ds_bpermute_b32 v189, v245, v189
	ds_bpermute_b32 v190, v245, v190
	ds_bpermute_b32 v191, v245, v191
	ds_bpermute_b32 v218, v245, v218
	ds_bpermute_b32 v219, v245, v219
	ds_bpermute_b32 v220, v245, v220
	ds_bpermute_b32 v221, v245, v221
	s_waitcnt lgkmcnt(0)
	v_pk_mul_f32 v[132:133], v[174:175], v[132:133] op_sel_hi:[0,1]
	v_pk_mul_f32 v[138:139], v[174:175], v[138:139] op_sel_hi:[0,1]
	v_pk_mul_f32 v[136:137], v[174:175], v[136:137] op_sel_hi:[0,1]
	v_pk_mul_f32 v[134:135], v[174:175], v[134:135] op_sel_hi:[0,1]
	v_pk_mul_f32 v[198:199], v[52:53], v[136:137]
	v_pk_mul_f32 v[200:201], v[54:55], v[138:139]
	v_mad_i64_i32 v[192:193], s[34:35], v172, s36, v[176:177]
	v_pk_fma_f32 v[200:201], v[62:63], v[134:135], v[200:201] neg_lo:[0,0,1] neg_hi:[0,0,1]
	v_pk_fma_f32 v[198:199], v[60:61], v[132:133], v[198:199] neg_lo:[0,0,1] neg_hi:[0,0,1]
	v_pk_mul_f32 v[204:205], v[60:61], v[136:137]
	v_pk_mul_f32 v[208:209], v[62:63], v[138:139]
	v_lshl_add_u64 v[192:193], v[192:193], 0, v[178:179]
	v_pk_fma_f32 v[208:209], v[54:55], v[134:135], v[208:209]
	v_pk_fma_f32 v[204:205], v[52:53], v[132:133], v[204:205]
	v_cvt_pk_bf16_f32 v228, v198, v199
	v_cvt_pk_bf16_f32 v229, v200, v201
	s_nop 0
	v_cvt_pk_bf16_f32 v230, v204, v205
	v_cvt_pk_bf16_f32 v231, v208, v209
	s_nop 1
	v_permlane16_swap_b32_e32 v228, v230
	v_permlane16_swap_b32_e32 v229, v231
	global_store_dwordx4 v[192:193], v[228:231], off
	v_pk_mul_f32 v[198:199], v[56:57], v[136:137]
	v_pk_mul_f32 v[200:201], v[58:59], v[138:139]
	v_pk_mul_f32 v[136:137], v[64:65], v[136:137]
	v_pk_fma_f32 v[200:201], v[66:67], v[134:135], v[200:201] neg_lo:[0,0,1] neg_hi:[0,0,1]
	v_pk_fma_f32 v[198:199], v[64:65], v[132:133], v[198:199] neg_lo:[0,0,1] neg_hi:[0,0,1]
	v_pk_mul_f32 v[138:139], v[66:67], v[138:139]
	v_pk_fma_f32 v[132:133], v[56:57], v[132:133], v[136:137]
	v_cvt_pk_bf16_f32 v232, v198, v199
	v_cvt_pk_bf16_f32 v233, v200, v201
	v_pk_fma_f32 v[134:135], v[58:59], v[134:135], v[138:139]
	v_cvt_pk_bf16_f32 v234, v132, v133
	v_pk_mul_f32 v[138:139], v[174:175], v[144:145] op_sel_hi:[0,1]
	v_cvt_pk_bf16_f32 v235, v134, v135
	s_nop 1
	v_permlane16_swap_b32_e32 v232, v234
	v_permlane16_swap_b32_e32 v233, v235
	global_store_dwordx4 v[192:193], v[232:235], off offset:256
	v_pk_mul_f32 v[136:137], v[174:175], v[146:147] op_sel_hi:[0,1]
	v_pk_mul_f32 v[132:133], v[174:175], v[140:141] op_sel_hi:[0,1]
	v_pk_mul_f32 v[134:135], v[174:175], v[142:143] op_sel_hi:[0,1]
	v_pk_mul_f32 v[142:143], v[36:37], v[138:139]
	v_pk_mul_f32 v[144:145], v[38:39], v[136:137]
	v_mad_i64_i32 v[140:141], s[34:35], v170, s36, v[176:177]
	v_pk_fma_f32 v[144:145], v[46:47], v[134:135], v[144:145] neg_lo:[0,0,1] neg_hi:[0,0,1]
	v_pk_fma_f32 v[142:143], v[44:45], v[132:133], v[142:143] neg_lo:[0,0,1] neg_hi:[0,0,1]
	v_pk_mul_f32 v[146:147], v[44:45], v[138:139]
	v_pk_mul_f32 v[192:193], v[46:47], v[136:137]
	v_lshl_add_u64 v[140:141], v[140:141], 0, v[178:179]
	v_pk_fma_f32 v[192:193], v[38:39], v[134:135], v[192:193]
	v_pk_fma_f32 v[146:147], v[36:37], v[132:133], v[146:147]
	v_cvt_pk_bf16_f32 v236, v142, v143
	v_cvt_pk_bf16_f32 v237, v144, v145
	s_nop 0
	v_cvt_pk_bf16_f32 v238, v146, v147
	v_cvt_pk_bf16_f32 v239, v192, v193
	s_nop 1
	v_permlane16_swap_b32_e32 v236, v238
	v_permlane16_swap_b32_e32 v237, v239
	global_store_dwordx4 v[140:141], v[236:239], off
	v_pk_mul_f32 v[142:143], v[40:41], v[138:139]
	v_pk_mul_f32 v[144:145], v[42:43], v[136:137]
	v_pk_mul_f32 v[138:139], v[48:49], v[138:139]
	v_pk_mul_f32 v[136:137], v[50:51], v[136:137]
	v_pk_fma_f32 v[144:145], v[50:51], v[134:135], v[144:145] neg_lo:[0,0,1] neg_hi:[0,0,1]
; #define PG8_ST8(rs, b0, p, v) __builtin_amdgcn_raw_buffer_store_b64(v, rs, (int)((const char*)(p) - (const char*)(b0)), 0, 16)
; __device__ __forceinline__ unsigned cvt_pk_bf16(float lo, float hi) { unsigned r; asm volatile("v_cvt_pk_bf16_f32 %0, %1, %2" : "=v"(r) : "v"(lo), "v"(hi)); return r; }
;     __device__ __forceinline__ void operator()(const f32x4 (&acc)[2][2][4][2], const Unit& u, int wr, int wc, int fr, int fq) const {
;     ...
;                 for (int m = 0; m < 4; ++m) { const int row = row0 + ai * HALF + m * 16;
;                     const f32x4 cc = c4[m] * sc, ss = s4[m] * sc;
;                     bf16_t* rowp = P + (size_t)row * ldp + col0;
; #pragma unroll
;                     for (int bj = 0; bj < 2; ++bj) { const f32x4 x1 = acc[ai][bj][m][0], x2 = acc[ai][bj][m][1]; const f32x4 o1 = x1 * cc - x2 * ss, o2 = x2 * cc + x1 * ss;
;                         u32x2 w1, w2; w1.x = cvt_pk_bf16(o1[0], o1[1]); w1.y = cvt_pk_bf16(o1[2], o1[3]); w2.x = cvt_pk_bf16(o2[0], o2[1]); w2.y = cvt_pk_bf16(o2[2], o2[3]);
;                         PG8_ST8(rsp_, P, rowp + bj * HALF, w1); PG8_ST8(rsp_, P, rowp + bj * HALF + 32, w2); } }
	v_pk_fma_f32 v[142:143], v[48:49], v[132:133], v[142:143] neg_lo:[0,0,1] neg_hi:[0,0,1]
	v_pk_fma_f32 v[134:135], v[42:43], v[134:135], v[136:137]
	v_pk_fma_f32 v[132:133], v[40:41], v[132:133], v[138:139]
	v_cvt_pk_bf16_f32 v240, v142, v143
	v_cvt_pk_bf16_f32 v241, v144, v145
	v_pk_mul_f32 v[138:139], v[174:175], v[184:185] op_sel_hi:[0,1]
	v_cvt_pk_bf16_f32 v242, v132, v133
	v_cvt_pk_bf16_f32 v243, v134, v135
	s_nop 1
	v_permlane16_swap_b32_e32 v240, v242
	v_permlane16_swap_b32_e32 v241, v243
	global_store_dwordx4 v[140:141], v[240:243], off offset:256
	v_pk_mul_f32 v[136:137], v[174:175], v[186:187] op_sel_hi:[0,1]
	v_pk_mul_f32 v[132:133], v[174:175], v[180:181] op_sel_hi:[0,1]
	v_pk_mul_f32 v[134:135], v[174:175], v[182:183] op_sel_hi:[0,1]
	v_pk_mul_f32 v[142:143], v[20:21], v[138:139]
	v_pk_mul_f32 v[144:145], v[22:23], v[136:137]
	v_mad_i64_i32 v[140:141], s[34:35], v168, s36, v[176:177]
	v_pk_fma_f32 v[144:145], v[30:31], v[134:135], v[144:145] neg_lo:[0,0,1] neg_hi:[0,0,1]
	v_pk_fma_f32 v[142:143], v[28:29], v[132:133], v[142:143] neg_lo:[0,0,1] neg_hi:[0,0,1]
	v_pk_mul_f32 v[146:147], v[28:29], v[138:139]
	v_pk_mul_f32 v[180:181], v[30:31], v[136:137]
	v_lshl_add_u64 v[140:141], v[140:141], 0, v[178:179]
	v_pk_fma_f32 v[180:181], v[22:23], v[134:135], v[180:181]
	v_pk_fma_f32 v[146:147], v[20:21], v[132:133], v[146:147]
	v_cvt_pk_bf16_f32 v228, v142, v143
	v_cvt_pk_bf16_f32 v229, v144, v145
	s_nop 0
	v_cvt_pk_bf16_f32 v230, v146, v147
	v_cvt_pk_bf16_f32 v231, v180, v181
	s_nop 1
	v_permlane16_swap_b32_e32 v228, v230
	v_permlane16_swap_b32_e32 v229, v231
	global_store_dwordx4 v[140:141], v[228:231], off
	v_pk_mul_f32 v[142:143], v[24:25], v[138:139]
	v_pk_mul_f32 v[144:145], v[26:27], v[136:137]
	v_pk_mul_f32 v[138:139], v[32:33], v[138:139]
	v_pk_mul_f32 v[136:137], v[34:35], v[136:137]
	v_pk_fma_f32 v[144:145], v[34:35], v[134:135], v[144:145] neg_lo:[0,0,1] neg_hi:[0,0,1]
	v_pk_fma_f32 v[142:143], v[32:33], v[132:133], v[142:143] neg_lo:[0,0,1] neg_hi:[0,0,1]
	v_pk_fma_f32 v[134:135], v[26:27], v[134:135], v[136:137]
	v_pk_fma_f32 v[132:133], v[24:25], v[132:133], v[138:139]
	v_cvt_pk_bf16_f32 v232, v142, v143
	v_cvt_pk_bf16_f32 v233, v144, v145
	v_pk_mul_f32 v[138:139], v[174:175], v[218:219] op_sel_hi:[0,1]
	v_cvt_pk_bf16_f32 v234, v132, v133
	v_cvt_pk_bf16_f32 v235, v134, v135
	s_nop 1
	v_permlane16_swap_b32_e32 v232, v234
	v_permlane16_swap_b32_e32 v233, v235
	global_store_dwordx4 v[140:141], v[232:235], off offset:256
	v_pk_mul_f32 v[136:137], v[174:175], v[220:221] op_sel_hi:[0,1]
	v_pk_mul_f32 v[132:133], v[174:175], v[188:189] op_sel_hi:[0,1]
	v_pk_mul_f32 v[134:135], v[174:175], v[190:191] op_sel_hi:[0,1]
	v_pk_mul_f32 v[142:143], v[4:5], v[138:139]
	v_pk_mul_f32 v[144:145], v[6:7], v[136:137]
	v_mad_i64_i32 v[140:141], s[34:35], v166, s36, v[176:177]
	v_pk_fma_f32 v[144:145], v[14:15], v[134:135], v[144:145] neg_lo:[0,0,1] neg_hi:[0,0,1]
	v_pk_fma_f32 v[142:143], v[12:13], v[132:133], v[142:143] neg_lo:[0,0,1] neg_hi:[0,0,1]
	v_pk_mul_f32 v[146:147], v[12:13], v[138:139]
	v_pk_mul_f32 v[176:177], v[14:15], v[136:137]
	v_lshl_add_u64 v[140:141], v[140:141], 0, v[178:179]
	v_pk_fma_f32 v[176:177], v[6:7], v[134:135], v[176:177]
	v_pk_fma_f32 v[146:147], v[4:5], v[132:133], v[146:147]
	v_cvt_pk_bf16_f32 v236, v142, v143
	v_cvt_pk_bf16_f32 v237, v144, v145
	s_mov_b64 s[34:35], 0
	v_cvt_pk_bf16_f32 v238, v146, v147
	v_cvt_pk_bf16_f32 v239, v176, v177
	s_nop 1
	v_permlane16_swap_b32_e32 v236, v238
	v_permlane16_swap_b32_e32 v237, v239
	global_store_dwordx4 v[140:141], v[236:239], off
	v_pk_mul_f32 v[142:143], v[8:9], v[138:139]
	v_pk_mul_f32 v[144:145], v[10:11], v[136:137]
	v_pk_mul_f32 v[138:139], v[16:17], v[138:139]
	v_pk_mul_f32 v[136:137], v[18:19], v[136:137]
	v_pk_fma_f32 v[144:145], v[18:19], v[134:135], v[144:145] neg_lo:[0,0,1] neg_hi:[0,0,1]
	v_pk_fma_f32 v[142:143], v[16:17], v[132:133], v[142:143] neg_lo:[0,0,1] neg_hi:[0,0,1]
	v_pk_fma_f32 v[134:135], v[10:11], v[134:135], v[136:137]
	v_pk_fma_f32 v[132:133], v[8:9], v[132:133], v[138:139]
	v_cvt_pk_bf16_f32 v136, v142, v143
	v_cvt_pk_bf16_f32 v137, v144, v145
	s_nop 0
	v_cvt_pk_bf16_f32 v242, v132, v133
	v_cvt_pk_bf16_f32 v243, v134, v135
	v_mov_b32_e32 v240, v136
	v_mov_b32_e32 v241, v137
	s_nop 1
	v_permlane16_swap_b32_e32 v240, v242
	v_permlane16_swap_b32_e32 v241, v243
	global_store_dwordx4 v[140:141], v[240:243], off offset:256
